# Plucker write-side epilogue: Jw Jw^T chunk sums by half-fold (permlane32_swap+add) + 5 DPP steps on 11 regs instead of a 6-step scan of 21
# speedup vs baseline: 1.0098x; 1.0074x over previous
.LBB1_21:
	s_andn2_b64 vcc, exec, s[26:27]
	s_cbranch_vccnz .LBB1_25
	v_mov_b32_e32 v5, 0
	v_lshlrev_b64 v[2:3], 10, v[4:5]
	v_or_b32_e32 v2, v2, v30
	v_xor_b32_e32 v9, 0x80000000, v16
	v_lshlrev_b64 v[6:7], 5, v[2:3]
	v_lshl_add_u64 v[14:15], s[18:19], 0, v[6:7]
	v_cvt_pk_f16_f32 v6, v17, v9
	v_cvt_f32_f16_e32 v22, v6
	v_cvt_f32_f16_sdwa v23, v6 dst_sel:DWORD dst_unused:UNUSED_PAD src0_sel:WORD_1
	v_mov_b32_e32 v8, v17
	v_xor_b32_e32 v18, 0x80000000, v13
	global_store_dwordx4 v[14:15], v[8:11], off
	v_mov_b32_e32 v19, v12
	v_mov_b32_e32 v20, v5
	v_mov_b32_e32 v21, v5
	v_pk_add_f32 v[8:9], v[8:9], v[22:23] neg_lo:[0,1] neg_hi:[0,1]
	v_cvt_pk_f16_f32 v7, v10, v11
	s_mov_b32 s26, 0x44800000
	global_store_dwordx4 v[14:15], v[18:21], off offset:16
	v_cvt_f32_f16_e32 v14, v7
	v_cvt_f32_f16_sdwa v15, v7 dst_sel:DWORD dst_unused:UNUSED_PAD src0_sel:WORD_1
	v_pk_mul_f32 v[8:9], v[8:9], s[26:27] op_sel_hi:[1,0]
	v_lshlrev_b64 v[2:3], 6, v[2:3]
	v_cvt_pk_f16_f32 v9, v8, v9
	v_cvt_pk_f16_f32 v8, v18, v12
	v_cvt_f32_f16_e32 v22, v8
	v_cvt_f32_f16_sdwa v23, v8 dst_sel:DWORD dst_unused:UNUSED_PAD src0_sel:WORD_1
	v_pk_add_f32 v[14:15], v[10:11], v[14:15] neg_lo:[0,1] neg_hi:[0,1]
	v_lshl_add_u64 v[2:3], s[16:17], 0, v[2:3]
	v_pk_mul_f32 v[14:15], v[14:15], s[26:27] op_sel_hi:[1,0]
	v_mov_b32_e32 v34, v8
	v_cvt_pk_f16_f32 v20, v14, v15
	v_pk_add_f32 v[14:15], v[18:19], v[22:23] neg_lo:[0,1] neg_hi:[0,1]
	v_mov_b32_e32 v22, v6
	v_pk_mul_f32 v[14:15], v[14:15], s[26:27] op_sel_hi:[1,0]
	v_mov_b32_e32 v23, v7
	v_cvt_pk_f16_f32 v21, v14, v15
	v_mov_b32_e32 v35, v5
	v_mov_b32_e32 v36, v5
	v_mov_b32_e32 v37, v5
	global_store_dwordx4 v[2:3], v[6:9], off
	global_store_dwordx4 v[2:3], v[20:23], off offset:16
	global_store_dwordx4 v[2:3], v[34:37], off offset:32
	v_mov_b32_e32 v6, v5
	v_mov_b32_e32 v7, v5
	v_mov_b32_e32 v8, v5
	v_mov_b32_e32 v9, v5
	global_store_dwordx4 v[2:3], v[6:9], off offset:48
	v_mul_f32_e64 v23, v17, -v16
	v_mul_f32_e32 v24, v17, v10
	v_pk_mul_f32 v[8:9], v[16:17], v[16:17]
	v_mul_f32_e32 v25, v17, v11
	v_mul_f32_e64 v6, v17, -v13
	v_mul_f32_e32 v7, v17, v12
	v_mul_f32_e64 v17, v10, -v16
	v_mul_f32_e64 v18, v11, -v16
	v_mul_f32_e32 v19, v16, v13
	v_mul_f32_e64 v20, v12, -v16
	v_pk_mul_f32 v[28:29], v[10:11], v[10:11]
	v_mul_f32_e32 v14, v10, v11
	v_mul_f32_e64 v15, v10, -v13
	v_mul_f32_e32 v16, v10, v12
	v_mul_f32_e64 v10, v11, -v13
	v_mul_f32_e32 v11, v11, v12
	v_pk_mul_f32 v[2:3], v[12:13], v[12:13]
	v_mul_f32_e64 v13, v12, -v13
	v_mov_b32_e32 v36, 0
	s_nop 1
	v_permlane32_swap_b32_e32 v9, v23
	v_permlane32_swap_b32_e32 v24, v25
	v_permlane32_swap_b32_e32 v6, v7
	v_permlane32_swap_b32_e32 v8, v17
	v_permlane32_swap_b32_e32 v18, v19
	v_permlane32_swap_b32_e32 v20, v28
	v_permlane32_swap_b32_e32 v14, v15
	v_permlane32_swap_b32_e32 v16, v29
	v_permlane32_swap_b32_e32 v10, v11
	v_permlane32_swap_b32_e32 v3, v13
	v_permlane32_swap_b32_e32 v2, v36
	v_add_f32_e32 v9, v9, v23
	v_add_f32_e32 v24, v24, v25
	v_add_f32_e32 v6, v6, v7
	v_add_f32_e32 v8, v8, v17
	v_add_f32_e32 v18, v18, v19
	v_add_f32_e32 v20, v20, v28
	v_add_f32_e32 v14, v14, v15
	v_add_f32_e32 v16, v16, v29
	v_add_f32_e32 v10, v10, v11
	v_add_f32_e32 v3, v3, v13
	v_add_f32_e32 v2, v2, v36
	v_add_f32_dpp v9, v9, v9 row_shr:1 row_mask:0xf bank_mask:0xf bound_ctrl:1
	v_add_f32_dpp v24, v24, v24 row_shr:1 row_mask:0xf bank_mask:0xf bound_ctrl:1
	v_add_f32_dpp v6, v6, v6 row_shr:1 row_mask:0xf bank_mask:0xf bound_ctrl:1
	v_add_f32_dpp v8, v8, v8 row_shr:1 row_mask:0xf bank_mask:0xf bound_ctrl:1
	v_add_f32_dpp v18, v18, v18 row_shr:1 row_mask:0xf bank_mask:0xf bound_ctrl:1
	v_add_f32_dpp v20, v20, v20 row_shr:1 row_mask:0xf bank_mask:0xf bound_ctrl:1
	v_add_f32_dpp v14, v14, v14 row_shr:1 row_mask:0xf bank_mask:0xf bound_ctrl:1
	v_add_f32_dpp v16, v16, v16 row_shr:1 row_mask:0xf bank_mask:0xf bound_ctrl:1
	v_add_f32_dpp v10, v10, v10 row_shr:1 row_mask:0xf bank_mask:0xf bound_ctrl:1
	v_add_f32_dpp v3, v3, v3 row_shr:1 row_mask:0xf bank_mask:0xf bound_ctrl:1
	v_add_f32_dpp v2, v2, v2 row_shr:1 row_mask:0xf bank_mask:0xf bound_ctrl:1
	v_add_f32_dpp v9, v9, v9 row_shr:2 row_mask:0xf bank_mask:0xf bound_ctrl:1
	v_add_f32_dpp v24, v24, v24 row_shr:2 row_mask:0xf bank_mask:0xf bound_ctrl:1
	v_add_f32_dpp v6, v6, v6 row_shr:2 row_mask:0xf bank_mask:0xf bound_ctrl:1
	v_add_f32_dpp v8, v8, v8 row_shr:2 row_mask:0xf bank_mask:0xf bound_ctrl:1
	v_add_f32_dpp v18, v18, v18 row_shr:2 row_mask:0xf bank_mask:0xf bound_ctrl:1
	v_add_f32_dpp v20, v20, v20 row_shr:2 row_mask:0xf bank_mask:0xf bound_ctrl:1
	v_add_f32_dpp v14, v14, v14 row_shr:2 row_mask:0xf bank_mask:0xf bound_ctrl:1
	v_add_f32_dpp v16, v16, v16 row_shr:2 row_mask:0xf bank_mask:0xf bound_ctrl:1
	v_add_f32_dpp v10, v10, v10 row_shr:2 row_mask:0xf bank_mask:0xf bound_ctrl:1
	v_add_f32_dpp v3, v3, v3 row_shr:2 row_mask:0xf bank_mask:0xf bound_ctrl:1
	v_add_f32_dpp v2, v2, v2 row_shr:2 row_mask:0xf bank_mask:0xf bound_ctrl:1
	v_add_f32_dpp v9, v9, v9 row_shr:4 row_mask:0xf bank_mask:0xf bound_ctrl:1
	v_add_f32_dpp v24, v24, v24 row_shr:4 row_mask:0xf bank_mask:0xf bound_ctrl:1
	v_add_f32_dpp v6, v6, v6 row_shr:4 row_mask:0xf bank_mask:0xf bound_ctrl:1
	v_add_f32_dpp v8, v8, v8 row_shr:4 row_mask:0xf bank_mask:0xf bound_ctrl:1
	v_add_f32_dpp v18, v18, v18 row_shr:4 row_mask:0xf bank_mask:0xf bound_ctrl:1
	v_add_f32_dpp v20, v20, v20 row_shr:4 row_mask:0xf bank_mask:0xf bound_ctrl:1
	v_add_f32_dpp v14, v14, v14 row_shr:4 row_mask:0xf bank_mask:0xf bound_ctrl:1
	v_add_f32_dpp v16, v16, v16 row_shr:4 row_mask:0xf bank_mask:0xf bound_ctrl:1
	v_add_f32_dpp v10, v10, v10 row_shr:4 row_mask:0xf bank_mask:0xf bound_ctrl:1
	v_add_f32_dpp v3, v3, v3 row_shr:4 row_mask:0xf bank_mask:0xf bound_ctrl:1
	v_add_f32_dpp v2, v2, v2 row_shr:4 row_mask:0xf bank_mask:0xf bound_ctrl:1
	v_add_f32_dpp v9, v9, v9 row_shr:8 row_mask:0xf bank_mask:0xf bound_ctrl:1
	v_add_f32_dpp v24, v24, v24 row_shr:8 row_mask:0xf bank_mask:0xf bound_ctrl:1
	v_add_f32_dpp v6, v6, v6 row_shr:8 row_mask:0xf bank_mask:0xf bound_ctrl:1
	v_add_f32_dpp v8, v8, v8 row_shr:8 row_mask:0xf bank_mask:0xf bound_ctrl:1
	v_add_f32_dpp v18, v18, v18 row_shr:8 row_mask:0xf bank_mask:0xf bound_ctrl:1
	v_add_f32_dpp v20, v20, v20 row_shr:8 row_mask:0xf bank_mask:0xf bound_ctrl:1
	v_add_f32_dpp v14, v14, v14 row_shr:8 row_mask:0xf bank_mask:0xf bound_ctrl:1
	v_add_f32_dpp v16, v16, v16 row_shr:8 row_mask:0xf bank_mask:0xf bound_ctrl:1
	v_add_f32_dpp v10, v10, v10 row_shr:8 row_mask:0xf bank_mask:0xf bound_ctrl:1
	v_add_f32_dpp v3, v3, v3 row_shr:8 row_mask:0xf bank_mask:0xf bound_ctrl:1
	v_add_f32_dpp v2, v2, v2 row_shr:8 row_mask:0xf bank_mask:0xf bound_ctrl:1
	v_add_f32_dpp v9, v9, v9 row_bcast:15 row_mask:0xa bank_mask:0xf
	v_add_f32_dpp v24, v24, v24 row_bcast:15 row_mask:0xa bank_mask:0xf
	v_add_f32_dpp v6, v6, v6 row_bcast:15 row_mask:0xa bank_mask:0xf
	v_add_f32_dpp v8, v8, v8 row_bcast:15 row_mask:0xa bank_mask:0xf
	v_add_f32_dpp v18, v18, v18 row_bcast:15 row_mask:0xa bank_mask:0xf
	v_add_f32_dpp v20, v20, v20 row_bcast:15 row_mask:0xa bank_mask:0xf
	v_add_f32_dpp v14, v14, v14 row_bcast:15 row_mask:0xa bank_mask:0xf
	v_add_f32_dpp v16, v16, v16 row_bcast:15 row_mask:0xa bank_mask:0xf
	v_add_f32_dpp v10, v10, v10 row_bcast:15 row_mask:0xa bank_mask:0xf
	v_add_f32_dpp v3, v3, v3 row_bcast:15 row_mask:0xa bank_mask:0xf
	v_add_f32_dpp v2, v2, v2 row_bcast:15 row_mask:0xa bank_mask:0xf
	s_nop 1
	v_and_b32_e32 v37, 31, v46
	v_cmp_eq_u32_e64 s[52:53], 31, v37
	s_and_saveexec_b64 s[26:27], s[52:53]
	s_cbranch_execz .LBB1_24
	v_lshl_or_b32 v4, v4, 4, s28
	s_movk_i32 s30, 0x60
	v_mov_b64_e32 v[34:35], s[22:23]
	v_mad_u64_u32 v[34:35], s[30:31], v4, s30, v[34:35]
	v_lshrrev_b32_e32 v37, 5, v46
	v_lshlrev_b32_e32 v36, 2, v37
	v_mov_b32_e32 v37, 0
	v_lshl_add_u64 v[34:35], v[34:35], 0, v[36:37]
	global_store_dword v[34:35], v9, off
	global_store_dword v[34:35], v24, off offset:8
	global_store_dword v[34:35], v6, off offset:16
	global_store_dword v[34:35], v8, off offset:24
	global_store_dword v[34:35], v18, off offset:32
	global_store_dword v[34:35], v20, off offset:40
	global_store_dword v[34:35], v14, off offset:48
	global_store_dword v[34:35], v16, off offset:56
	global_store_dword v[34:35], v10, off offset:64
	global_store_dword v[34:35], v3, off offset:72
	global_store_dword v[34:35], v2, off offset:80

.LBB1_27:
	s_andn2_b64 vcc, exec, s[6:7]
	s_cbranch_vccnz .LBB1_31
	v_mov_b32_e32 v5, 0
	v_lshlrev_b64 v[2:3], 10, v[4:5]
	v_or_b32_e32 v2, v2, v30
	v_xor_b32_e32 v9, 0x80000000, v16
	v_lshlrev_b64 v[6:7], 5, v[2:3]
	v_lshl_add_u64 v[14:15], s[18:19], 0, v[6:7]
	v_cvt_pk_f16_f32 v6, v17, v9
	v_cvt_f32_f16_e32 v22, v6
	v_cvt_f32_f16_sdwa v23, v6 dst_sel:DWORD dst_unused:UNUSED_PAD src0_sel:WORD_1
	v_mov_b32_e32 v8, v17
	v_xor_b32_e32 v18, 0x80000000, v13
	global_store_dwordx4 v[14:15], v[8:11], off
	v_mov_b32_e32 v19, v12
	v_mov_b32_e32 v20, v5
	v_mov_b32_e32 v21, v5
	v_pk_add_f32 v[8:9], v[8:9], v[22:23] neg_lo:[0,1] neg_hi:[0,1]
	v_cvt_pk_f16_f32 v7, v10, v11
	s_mov_b32 s6, 0x44800000
	global_store_dwordx4 v[14:15], v[18:21], off offset:16
	v_cvt_f32_f16_e32 v14, v7
	v_cvt_f32_f16_sdwa v15, v7 dst_sel:DWORD dst_unused:UNUSED_PAD src0_sel:WORD_1
	v_pk_mul_f32 v[8:9], v[8:9], s[6:7] op_sel_hi:[1,0]
	v_lshlrev_b64 v[2:3], 6, v[2:3]
	v_cvt_pk_f16_f32 v9, v8, v9
	v_cvt_pk_f16_f32 v8, v18, v12
	v_cvt_f32_f16_e32 v22, v8
	v_cvt_f32_f16_sdwa v23, v8 dst_sel:DWORD dst_unused:UNUSED_PAD src0_sel:WORD_1
	v_pk_add_f32 v[14:15], v[10:11], v[14:15] neg_lo:[0,1] neg_hi:[0,1]
	v_lshl_add_u64 v[2:3], s[16:17], 0, v[2:3]
	v_pk_mul_f32 v[14:15], v[14:15], s[6:7] op_sel_hi:[1,0]
	v_mov_b32_e32 v24, v8
	v_cvt_pk_f16_f32 v20, v14, v15
	v_pk_add_f32 v[14:15], v[18:19], v[22:23] neg_lo:[0,1] neg_hi:[0,1]
	v_mov_b32_e32 v22, v6
	v_pk_mul_f32 v[14:15], v[14:15], s[6:7] op_sel_hi:[1,0]
	v_mov_b32_e32 v23, v7
	v_cvt_pk_f16_f32 v21, v14, v15
	v_mov_b32_e32 v25, v5
	v_mov_b32_e32 v26, v5
	v_mov_b32_e32 v27, v5
	global_store_dwordx4 v[2:3], v[6:9], off
	global_store_dwordx4 v[2:3], v[20:23], off offset:16
	global_store_dwordx4 v[2:3], v[24:27], off offset:32
	v_mov_b32_e32 v6, v5
	v_mov_b32_e32 v7, v5
	v_mov_b32_e32 v8, v5
	v_mov_b32_e32 v9, v5
	global_store_dwordx4 v[2:3], v[6:9], off offset:48
	v_mul_f32_e64 v23, v17, -v16
	v_mul_f32_e32 v24, v17, v10
	v_pk_mul_f32 v[8:9], v[16:17], v[16:17]
	v_mul_f32_e32 v25, v17, v11
	v_mul_f32_e64 v6, v17, -v13
	v_mul_f32_e32 v7, v17, v12
	v_mul_f32_e64 v17, v10, -v16
	v_mul_f32_e64 v18, v11, -v16
	v_mul_f32_e32 v19, v16, v13
	v_mul_f32_e64 v20, v12, -v16
	v_pk_mul_f32 v[26:27], v[10:11], v[10:11]
	v_mul_f32_e32 v14, v10, v11
	v_mul_f32_e64 v15, v10, -v13
	v_mul_f32_e32 v16, v10, v12
	v_mul_f32_e64 v10, v11, -v13
	v_mul_f32_e32 v11, v11, v12
	v_pk_mul_f32 v[2:3], v[12:13], v[12:13]
	v_mul_f32_e64 v13, v12, -v13
	v_mov_b32_e32 v36, 0
	s_nop 1
	v_permlane32_swap_b32_e32 v9, v23
	v_permlane32_swap_b32_e32 v24, v25
	v_permlane32_swap_b32_e32 v6, v7
	v_permlane32_swap_b32_e32 v8, v17
	v_permlane32_swap_b32_e32 v18, v19
	v_permlane32_swap_b32_e32 v20, v26
	v_permlane32_swap_b32_e32 v14, v15
	v_permlane32_swap_b32_e32 v16, v27
	v_permlane32_swap_b32_e32 v10, v11
	v_permlane32_swap_b32_e32 v3, v13
	v_permlane32_swap_b32_e32 v2, v36
	v_add_f32_e32 v9, v9, v23
	v_add_f32_e32 v24, v24, v25
	v_add_f32_e32 v6, v6, v7
	v_add_f32_e32 v8, v8, v17
	v_add_f32_e32 v18, v18, v19
	v_add_f32_e32 v20, v20, v26
	v_add_f32_e32 v14, v14, v15
	v_add_f32_e32 v16, v16, v27
	v_add_f32_e32 v10, v10, v11
	v_add_f32_e32 v3, v3, v13
	v_add_f32_e32 v2, v2, v36
	v_add_f32_dpp v9, v9, v9 row_shr:1 row_mask:0xf bank_mask:0xf bound_ctrl:1
	v_add_f32_dpp v24, v24, v24 row_shr:1 row_mask:0xf bank_mask:0xf bound_ctrl:1
	v_add_f32_dpp v6, v6, v6 row_shr:1 row_mask:0xf bank_mask:0xf bound_ctrl:1
	v_add_f32_dpp v8, v8, v8 row_shr:1 row_mask:0xf bank_mask:0xf bound_ctrl:1
	v_add_f32_dpp v18, v18, v18 row_shr:1 row_mask:0xf bank_mask:0xf bound_ctrl:1
	v_add_f32_dpp v20, v20, v20 row_shr:1 row_mask:0xf bank_mask:0xf bound_ctrl:1
	v_add_f32_dpp v14, v14, v14 row_shr:1 row_mask:0xf bank_mask:0xf bound_ctrl:1
	v_add_f32_dpp v16, v16, v16 row_shr:1 row_mask:0xf bank_mask:0xf bound_ctrl:1
	v_add_f32_dpp v10, v10, v10 row_shr:1 row_mask:0xf bank_mask:0xf bound_ctrl:1
	v_add_f32_dpp v3, v3, v3 row_shr:1 row_mask:0xf bank_mask:0xf bound_ctrl:1
	v_add_f32_dpp v2, v2, v2 row_shr:1 row_mask:0xf bank_mask:0xf bound_ctrl:1
	v_add_f32_dpp v9, v9, v9 row_shr:2 row_mask:0xf bank_mask:0xf bound_ctrl:1
	v_add_f32_dpp v24, v24, v24 row_shr:2 row_mask:0xf bank_mask:0xf bound_ctrl:1
	v_add_f32_dpp v6, v6, v6 row_shr:2 row_mask:0xf bank_mask:0xf bound_ctrl:1
	v_add_f32_dpp v8, v8, v8 row_shr:2 row_mask:0xf bank_mask:0xf bound_ctrl:1
	v_add_f32_dpp v18, v18, v18 row_shr:2 row_mask:0xf bank_mask:0xf bound_ctrl:1
	v_add_f32_dpp v20, v20, v20 row_shr:2 row_mask:0xf bank_mask:0xf bound_ctrl:1
	v_add_f32_dpp v14, v14, v14 row_shr:2 row_mask:0xf bank_mask:0xf bound_ctrl:1
	v_add_f32_dpp v16, v16, v16 row_shr:2 row_mask:0xf bank_mask:0xf bound_ctrl:1
	v_add_f32_dpp v10, v10, v10 row_shr:2 row_mask:0xf bank_mask:0xf bound_ctrl:1
	v_add_f32_dpp v3, v3, v3 row_shr:2 row_mask:0xf bank_mask:0xf bound_ctrl:1
	v_add_f32_dpp v2, v2, v2 row_shr:2 row_mask:0xf bank_mask:0xf bound_ctrl:1
	v_add_f32_dpp v9, v9, v9 row_shr:4 row_mask:0xf bank_mask:0xf bound_ctrl:1
	v_add_f32_dpp v24, v24, v24 row_shr:4 row_mask:0xf bank_mask:0xf bound_ctrl:1
	v_add_f32_dpp v6, v6, v6 row_shr:4 row_mask:0xf bank_mask:0xf bound_ctrl:1
	v_add_f32_dpp v8, v8, v8 row_shr:4 row_mask:0xf bank_mask:0xf bound_ctrl:1
	v_add_f32_dpp v18, v18, v18 row_shr:4 row_mask:0xf bank_mask:0xf bound_ctrl:1
	v_add_f32_dpp v20, v20, v20 row_shr:4 row_mask:0xf bank_mask:0xf bound_ctrl:1
	v_add_f32_dpp v14, v14, v14 row_shr:4 row_mask:0xf bank_mask:0xf bound_ctrl:1
	v_add_f32_dpp v16, v16, v16 row_shr:4 row_mask:0xf bank_mask:0xf bound_ctrl:1
	v_add_f32_dpp v10, v10, v10 row_shr:4 row_mask:0xf bank_mask:0xf bound_ctrl:1
	v_add_f32_dpp v3, v3, v3 row_shr:4 row_mask:0xf bank_mask:0xf bound_ctrl:1
	v_add_f32_dpp v2, v2, v2 row_shr:4 row_mask:0xf bank_mask:0xf bound_ctrl:1
	v_add_f32_dpp v9, v9, v9 row_shr:8 row_mask:0xf bank_mask:0xf bound_ctrl:1
	v_add_f32_dpp v24, v24, v24 row_shr:8 row_mask:0xf bank_mask:0xf bound_ctrl:1
	v_add_f32_dpp v6, v6, v6 row_shr:8 row_mask:0xf bank_mask:0xf bound_ctrl:1
	v_add_f32_dpp v8, v8, v8 row_shr:8 row_mask:0xf bank_mask:0xf bound_ctrl:1
	v_add_f32_dpp v18, v18, v18 row_shr:8 row_mask:0xf bank_mask:0xf bound_ctrl:1
	v_add_f32_dpp v20, v20, v20 row_shr:8 row_mask:0xf bank_mask:0xf bound_ctrl:1
	v_add_f32_dpp v14, v14, v14 row_shr:8 row_mask:0xf bank_mask:0xf bound_ctrl:1
	v_add_f32_dpp v16, v16, v16 row_shr:8 row_mask:0xf bank_mask:0xf bound_ctrl:1
	v_add_f32_dpp v10, v10, v10 row_shr:8 row_mask:0xf bank_mask:0xf bound_ctrl:1
	v_add_f32_dpp v3, v3, v3 row_shr:8 row_mask:0xf bank_mask:0xf bound_ctrl:1
	v_add_f32_dpp v2, v2, v2 row_shr:8 row_mask:0xf bank_mask:0xf bound_ctrl:1
	v_add_f32_dpp v9, v9, v9 row_bcast:15 row_mask:0xa bank_mask:0xf
	v_add_f32_dpp v24, v24, v24 row_bcast:15 row_mask:0xa bank_mask:0xf
	v_add_f32_dpp v6, v6, v6 row_bcast:15 row_mask:0xa bank_mask:0xf
	v_add_f32_dpp v8, v8, v8 row_bcast:15 row_mask:0xa bank_mask:0xf
	v_add_f32_dpp v18, v18, v18 row_bcast:15 row_mask:0xa bank_mask:0xf
	v_add_f32_dpp v20, v20, v20 row_bcast:15 row_mask:0xa bank_mask:0xf
	v_add_f32_dpp v14, v14, v14 row_bcast:15 row_mask:0xa bank_mask:0xf
	v_add_f32_dpp v16, v16, v16 row_bcast:15 row_mask:0xa bank_mask:0xf
	v_add_f32_dpp v10, v10, v10 row_bcast:15 row_mask:0xa bank_mask:0xf
	v_add_f32_dpp v3, v3, v3 row_bcast:15 row_mask:0xa bank_mask:0xf
	v_add_f32_dpp v2, v2, v2 row_bcast:15 row_mask:0xa bank_mask:0xf
	s_nop 1
	v_and_b32_e32 v37, 31, v46
	v_cmp_eq_u32_e64 s[52:53], 31, v37
	s_and_saveexec_b64 s[6:7], s[52:53]
	s_cbranch_execz .LBB1_30
	v_lshl_or_b32 v4, v4, 4, s28
	s_movk_i32 s4, 0x60
	v_mov_b64_e32 v[28:29], s[22:23]
	v_mad_u64_u32 v[28:29], s[4:5], v4, s4, v[28:29]
	v_lshrrev_b32_e32 v37, 5, v46
	v_lshlrev_b32_e32 v36, 2, v37
	v_mov_b32_e32 v37, 0
	v_lshl_add_u64 v[28:29], v[28:29], 0, v[36:37]
	global_store_dword v[28:29], v9, off
	global_store_dword v[28:29], v24, off offset:8
	global_store_dword v[28:29], v6, off offset:16
	global_store_dword v[28:29], v8, off offset:24
	global_store_dword v[28:29], v18, off offset:32
	global_store_dword v[28:29], v20, off offset:40
	global_store_dword v[28:29], v14, off offset:48
	global_store_dword v[28:29], v16, off offset:56
	global_store_dword v[28:29], v10, off offset:64
	global_store_dword v[28:29], v3, off offset:72
	global_store_dword v[28:29], v2, off offset:80

amdhsa.kernels:
  - .agpr_count:     0
    .args:
      - .actual_access:  read_only
        .address_space:  global
        .offset:         0
        .size:           8
        .value_kind:     global_buffer
      - .actual_access:  read_only
        .address_space:  global
        .offset:         8
        .size:           8
        .value_kind:     global_buffer
      - .actual_access:  read_only
        .address_space:  global
        .offset:         16
        .size:           8
        .value_kind:     global_buffer
      - .actual_access:  read_only
        .address_space:  global
        .offset:         24
        .size:           8
        .value_kind:     global_buffer
      - .actual_access:  read_only
        .address_space:  global
        .offset:         32
        .size:           8
        .value_kind:     global_buffer
      - .actual_access:  read_only
        .address_space:  global
        .offset:         40
        .size:           8
        .value_kind:     global_buffer
      - .actual_access:  read_only
        .address_space:  global
        .offset:         48
        .size:           8
        .value_kind:     global_buffer
      - .address_space:  global
        .offset:         56
        .size:           8
        .value_kind:     global_buffer
      - .address_space:  global
        .offset:         64
        .size:           8
        .value_kind:     global_buffer
      - .actual_access:  read_only
        .address_space:  global
        .offset:         72
        .size:           8
        .value_kind:     global_buffer
      - .address_space:  global
        .offset:         80
        .size:           8
        .value_kind:     global_buffer
    .group_segment_fixed_size: 0
    .kernarg_segment_align: 8
    .kernarg_segment_size: 88
    .language:       OpenCL C
    .language_version:
      - 2
      - 0
    .max_flat_workgroup_size: 256
    .name:           _Z11prep_kernelPKfS0_S0_S0_S0_S0_S0_PDF16_S1_S1_S1_
    .private_segment_fixed_size: 0
    .sgpr_count:     23
    .sgpr_spill_count: 0
    .symbol:         _Z11prep_kernelPKfS0_S0_S0_S0_S0_S0_PDF16_S1_S1_S1_.kd
    .uniform_work_group_size: 1
    .uses_dynamic_stack: false
    .vgpr_count:     28
    .vgpr_spill_count: 0
    .wavefront_size: 64
  - .agpr_count:     0
    .args:
      - .offset:         0
        .size:           88
        .value_kind:     by_value
    .group_segment_fixed_size: 163840
    .kernarg_segment_align: 8
    .kernarg_segment_size: 88
    .language:       OpenCL C
    .language_version:
      - 2
      - 0
    .max_flat_workgroup_size: 512
    .name:           _Z12gemm1_kernel6G1Args
    .private_segment_fixed_size: 0
    .sgpr_count:     60
    .sgpr_spill_count: 0
    .symbol:         _Z12gemm1_kernel6G1Args.kd
    .uniform_work_group_size: 1
    .uses_dynamic_stack: false
    .vgpr_count:     240
    .vgpr_spill_count: 0
    .wavefront_size: 64
  - .agpr_count:     0
    .args:
      - .address_space:  global
        .offset:         0
        .size:           8
        .value_kind:     global_buffer
      - .address_space:  global
        .offset:         8
        .size:           8
        .value_kind:     global_buffer
      - .address_space:  global
        .offset:         16
        .size:           8
        .value_kind:     global_buffer
      - .actual_access:  read_only
        .address_space:  global
        .offset:         24
        .size:           8
        .value_kind:     global_buffer
      - .actual_access:  read_only
        .address_space:  global
        .offset:         32
        .size:           8
        .value_kind:     global_buffer
      - .actual_access:  read_only
        .address_space:  global
        .offset:         40
        .size:           8
        .value_kind:     global_buffer
      - .address_space:  global
        .offset:         48
        .size:           8
        .value_kind:     global_buffer
      - .actual_access:  read_only
        .address_space:  global
        .offset:         56
        .size:           8
        .value_kind:     global_buffer
      - .address_space:  global
        .offset:         64
        .size:           8
        .value_kind:     global_buffer
      - .actual_access:  read_only
        .address_space:  global
        .offset:         72
        .size:           8
        .value_kind:     global_buffer
      - .address_space:  global
        .offset:         80
        .size:           8
        .value_kind:     global_buffer
    .group_segment_fixed_size: 81920
    .kernarg_segment_align: 8
    .kernarg_segment_size: 88
    .language:       OpenCL C
    .language_version:
      - 2
      - 0
    .max_flat_workgroup_size: 512
    .name:           _Z11attn_kernelPKDF16_S0_S0_PKfS2_S2_S0_S2_PDF16_S2_S3_
    .private_segment_fixed_size: 0
    .sgpr_count:     71
    .sgpr_spill_count: 0
    .symbol:         _Z11attn_kernelPKDF16_S0_S0_PKfS2_S2_S0_S2_PDF16_S2_S3_.kd
    .uniform_work_group_size: 1
    .uses_dynamic_stack: false
    .vgpr_count:     126
    .vgpr_spill_count: 0
    .wavefront_size: 64
  - .agpr_count:     0
    .args:
      - .address_space:  global
        .offset:         0
        .size:           8
        .value_kind:     global_buffer
      - .address_space:  global
        .offset:         8
        .size:           8
        .value_kind:     global_buffer
      - .actual_access:  read_only
        .address_space:  global
        .offset:         16
        .size:           8
        .value_kind:     global_buffer
      - .actual_access:  write_only
        .address_space:  global
        .offset:         24
        .size:           8
        .value_kind:     global_buffer
    .group_segment_fixed_size: 122880
    .kernarg_segment_align: 8
    .kernarg_segment_size: 32
    .language:       OpenCL C
    .language_version:
      - 2
      - 0
    .max_flat_workgroup_size: 512
    .name:           _Z14outproj_kernelPKDF16_S0_PKfPf
    .private_segment_fixed_size: 0
    .sgpr_count:     31
    .sgpr_spill_count: 0
    .symbol:         _Z14outproj_kernelPKDF16_S0_PKfPf.kd
    .uniform_work_group_size: 1
    .uses_dynamic_stack: false
    .vgpr_count:     132
    .vgpr_spill_count: 0
    .wavefront_size: 64
